# speedup vs baseline: 1.0235x; 1.0235x over previous
_Z13select_kernelPK15HIP_vector_typeIjLj2EEPKfPf:
	s_lshr_b32 s3, s2, 3
	s_lshl_b32 s4, s2, 2
	s_mul_hi_u32 s2, s2, 0xaaaaaaab
	s_load_dwordx2 s[38:39], s[0:1], 0x0
	s_load_dwordx2 s[36:37], s[0:1], 0x10
	s_and_b32 s33, s4, 28
	s_lshr_b32 s2, s2, 5
	s_add_i32 s33, s33, s2
	s_mul_hi_u32 s2, s3, 0x2aaaaaab
	s_mul_i32 s2, s2, 6
	s_sub_i32 s46, s3, s2
	s_cmp_lg_u32 s46, 0
	s_cbranch_scc1 .Lk2_dt

.Lk2_dt:
	s_load_dwordx2 s[40:41], s[0:1], 0x8
	s_movk_i32 s0, 0x140
	v_cmp_gt_u32_e64 s[2:3], s0, v0
	s_mov_b64 s[0:1], 0
	s_and_saveexec_b64 s[4:5], s[2:3]
	s_cbranch_execz .LBB1_3
	s_mul_i32 s0, s33, 0x1388
	v_add_u32_e32 v2, s0, v0
	v_mov_b32_e32 v3, 0
	s_waitcnt lgkmcnt(0)
	v_lshl_add_u64 v[2:3], v[2:3], 3, s[38:39]
	global_load_dword v57, v[2:3], off offset:4
